# conv-loop exact vmcnt + P10 and P0 norm gain loads hoisted out of the row loops (no per-chunk vmcnt0 between stores)
# speedup vs baseline: 1.0249x; 1.0040x over previous
.LBB0_5:
	s_or_b64 exec, exec, s[4:5]
	v_readlane_b32 s2, v252, 0
	s_lshr_b32 s3, s2, 6
	s_lshl_b32 s2, s96, 3
	s_lshl_b32 s88, s43, 3
	s_add_i32 s90, s3, s2
	v_mov_b32_e32 v1, v0
	s_cmpk_lt_i32 s90, 0x4000
	s_cselect_b64 s[92:93], -1, 0
	s_cmpk_gt_i32 s90, 0x3fff
	v_mbcnt_lo_u32_b32 v228, -1, 0
	v_lshlrev_b32_e32 v100, 2, v1
	v_and_b32_e32 v101, 63, v1
	v_writelane_b32 v252, s3, 6
	s_cbranch_scc1 .LBB0_24
	v_mbcnt_hi_u32_b32 v2, -1, v228
	v_and_b32_e32 v3, 64, v2
	v_add_u32_e32 v3, 64, v3
	v_xor_b32_e32 v4, 32, v2
	v_cmp_lt_i32_e32 vcc, v4, v3
	s_add_u32 s2, s84, 0x4000000
	s_addc_u32 s3, s85, 0
	v_cndmask_b32_e32 v4, v2, v4, vcc
	v_lshlrev_b32_e32 v102, 2, v4
	v_xor_b32_e32 v4, 16, v2
	v_cmp_lt_i32_e32 vcc, v4, v3
	s_add_u32 s18, s84, 0x79800000
	v_and_b32_e32 v70, 0xfc, v100
	v_cndmask_b32_e32 v4, v2, v4, vcc
	v_lshlrev_b32_e32 v103, 2, v4
	v_xor_b32_e32 v4, 8, v2
	v_cmp_lt_i32_e32 vcc, v4, v3
	v_mov_b32_e32 v71, 0
	s_addc_u32 s19, s85, 0
	v_cndmask_b32_e32 v4, v2, v4, vcc
	v_lshlrev_b32_e32 v104, 2, v4
	v_xor_b32_e32 v4, 4, v2
	v_cmp_lt_i32_e32 vcc, v4, v3
	v_lshlrev_b32_e32 v10, 2, v70
	v_mov_b32_e32 v11, v71
	v_cndmask_b32_e32 v4, v2, v4, vcc
	v_lshlrev_b32_e32 v105, 2, v4
	v_xor_b32_e32 v4, 2, v2
	v_cmp_lt_i32_e32 vcc, v4, v3
	s_ashr_i32 s91, s90, 31
	s_lshl_b32 s6, s43, 4
	v_cndmask_b32_e32 v4, v2, v4, vcc
	v_lshlrev_b32_e32 v106, 2, v4
	v_xor_b32_e32 v4, 1, v2
	v_cmp_lt_i32_e32 vcc, v4, v3
	v_lshl_add_u64 v[72:73], s[50:51], 0, v[10:11]
	s_lshl_b64 s[4:5], s[90:91], 11
	v_cndmask_b32_e32 v2, v2, v4, vcc
	v_lshlrev_b32_e32 v107, 2, v2
	v_or_b32_e32 v2, 0x400, v70
	v_or_b32_e32 v4, 0x500, v70
	v_lshlrev_b32_e32 v10, 2, v2
	v_or_b32_e32 v6, 0x600, v70
	v_lshl_add_u64 v[74:75], s[50:51], 0, v[10:11]
	v_lshlrev_b32_e32 v10, 2, v4
	v_or_b32_e32 v82, s4, v70
	v_mov_b32_e32 v83, s5
	s_ashr_i32 s7, s6, 31
	s_lshl_b64 s[4:5], s[90:91], 12
	v_and_b32_e32 v3, 63, v1
	v_or_b32_e32 v8, 0x700, v70
	v_lshl_add_u64 v[76:77], s[50:51], 0, v[10:11]
	v_lshlrev_b32_e32 v10, 2, v6
	s_lshl_b64 s[8:9], s[6:7], 11
	v_lshl_or_b32 v84, v3, 3, s4
	v_mov_b32_e32 v85, s5
	s_lshl_b64 s[10:11], s[6:7], 12
	s_lshl_b64 s[4:5], s[90:91], 13
	v_lshl_add_u64 v[78:79], s[50:51], 0, v[10:11]
	v_lshlrev_b32_e32 v10, 2, v8
	s_add_u32 s4, s48, s4
	v_lshl_add_u64 v[80:81], s[50:51], 0, v[10:11]
	v_lshlrev_b32_e32 v10, 4, v3
	s_addc_u32 s5, s49, s5
	v_lshl_add_u64 v[10:11], s[4:5], 0, v[10:11]
	s_mov_b64 s[4:5], 0x1000
	v_lshl_add_u64 v[86:87], v[10:11], 0, s[4:5]
	s_lshl_b64 s[12:13], s[6:7], 13
	v_lshlrev_b32_e32 v108, 2, v70
	v_lshlrev_b32_e32 v109, 2, v2
	v_lshlrev_b32_e32 v110, 2, v4
	v_lshlrev_b32_e32 v111, 2, v6
	v_lshlrev_b32_e32 v112, 2, v8
	v_mov_b32_e32 v113, 0x3727c5ac
	s_brev_b32 s7, 32
	s_mov_b32 s20, s90
	global_load_dwordx4 v[120:123], v[72:73], off offset:1024
	global_load_dwordx4 v[124:127], v[72:73], off offset:2048
	global_load_dwordx4 v[128:131], v[72:73], off offset:3072
	global_load_dwordx4 v[132:135], v[74:75], off
	global_load_dwordx4 v[136:139], v[76:77], off
	global_load_dwordx4 v[140:143], v[78:79], off
	global_load_dwordx4 v[144:147], v[80:81], off
	s_branch .LBB0_8

.LBB0_10:
	v_mov_b32_e32 v97, v96
	v_pk_mul_f32 v[38:39], v[38:39], v[96:97]
	v_mov_b32_e32 v66, 0
	v_mov_b32_e32 v62, v96
	v_mov_b32_e32 v63, v96
	v_pk_mul_f32 v[40:41], v[40:41], v[62:63]
	v_add_co_u32_e32 v64, vcc, 0x79800000, v94
	v_pk_mul_f32 v[38:39], v[38:39], v[120:121]
	s_nop 0
	v_cvt_pk_fp8_f32 v66, v38, v39
	v_pk_mul_f32 v[40:41], v[40:41], v[122:123]
	v_cvt_pk_bf16_f32 v38, v38, v39
	v_cvt_pk_bf16_f32 v39, v40, v41
	v_cvt_pk_fp8_f32 v66, v40, v41 op_sel:[0,0,1]
	global_store_dwordx2 v[98:99], v[38:39], off offset:512
	v_addc_co_u32_e32 v65, vcc, 0, v95, vcc
	v_cndmask_b32_e64 v38, 0, 1, s[16:17]
	v_cmp_ne_u32_e64 s[4:5], 1, v38
	s_andn2_b64 vcc, exec, s[16:17]
	global_store_dword v[64:65], v66, off offset:256
	s_cbranch_vccnz .LBB0_12
	v_pk_mul_f32 v[40:41], v[58:59], v[90:91]
	v_mov_b32_e32 v38, v90
	v_pk_mul_f32 v[40:41], v[40:41], v[120:121]
	v_mov_b32_e32 v50, 0
	v_cvt_pk_fp8_f32 v50, v40, v41
	v_mov_b32_e32 v39, v90
	v_pk_mul_f32 v[38:39], v[60:61], v[38:39]
	v_cvt_pk_bf16_f32 v40, v40, v41
	v_pk_mul_f32 v[38:39], v[38:39], v[122:123]
	s_nop 0
	v_cvt_pk_fp8_f32 v50, v38, v39 op_sel:[0,0,1]
	v_cvt_pk_bf16_f32 v41, v38, v39
	global_store_dwordx2 v114, v[40:41], s[14:15] offset:512
	global_store_dword v[88:89], v50, off offset:256
.LBB0_12:
	v_pk_mul_f32 v[34:35], v[34:35], v[96:97]
	v_mov_b32_e32 v58, 0
	v_pk_mul_f32 v[36:37], v[36:37], v[62:63]
	v_add_co_u32_e32 v50, vcc, 0x4000000, v92
	v_pk_mul_f32 v[34:35], v[34:35], v[124:125]
	s_nop 0
	v_cvt_pk_fp8_f32 v58, v34, v35
	v_pk_mul_f32 v[36:37], v[36:37], v[126:127]
	v_addc_co_u32_e32 v51, vcc, 0, v93, vcc
	v_cvt_pk_fp8_f32 v58, v36, v37 op_sel:[0,0,1]
	v_add_co_u32_e32 v52, vcc, 0x79800000, v94
	v_cvt_pk_bf16_f32 v34, v34, v35
	s_nop 0
	v_addc_co_u32_e32 v53, vcc, 0, v95, vcc
	v_cvt_pk_bf16_f32 v35, v36, v37
	s_and_b64 vcc, exec, s[4:5]
	global_store_dwordx2 v[50:51], v[34:35], off offset:1024
	global_store_dword v[52:53], v58, off offset:512
	s_cbranch_vccnz .LBB0_14
	v_pk_mul_f32 v[36:37], v[54:55], v[90:91]
	v_mov_b32_e32 v34, v90
	v_pk_mul_f32 v[36:37], v[36:37], v[124:125]
	v_mov_b32_e32 v38, 0
	v_cvt_pk_fp8_f32 v38, v36, v37
	v_mov_b32_e32 v35, v90
	v_pk_mul_f32 v[34:35], v[56:57], v[34:35]
	v_cvt_pk_bf16_f32 v36, v36, v37
	v_pk_mul_f32 v[34:35], v[34:35], v[126:127]
	s_nop 0
	v_cvt_pk_fp8_f32 v38, v34, v35 op_sel:[0,0,1]
	v_cvt_pk_bf16_f32 v37, v34, v35
	global_store_dwordx2 v114, v[36:37], s[14:15] offset:1024
	global_store_dword v[88:89], v38, off offset:512
.LBB0_14:
	v_pk_mul_f32 v[26:27], v[26:27], v[96:97]
	v_mov_b32_e32 v52, 0
	v_mov_b32_e32 v38, v96
	v_mov_b32_e32 v39, v96
	v_pk_mul_f32 v[28:29], v[28:29], v[38:39]
	v_add_co_u32_e32 v40, vcc, 0x4000000, v92
	v_pk_mul_f32 v[26:27], v[26:27], v[128:129]
	s_nop 0
	v_cvt_pk_fp8_f32 v52, v26, v27
	v_pk_mul_f32 v[28:29], v[28:29], v[130:131]
	v_addc_co_u32_e32 v41, vcc, 0, v93, vcc
	v_cvt_pk_fp8_f32 v52, v28, v29 op_sel:[0,0,1]
	v_add_co_u32_e32 v50, vcc, 0x79800000, v94
	v_cvt_pk_bf16_f32 v26, v26, v27
	s_nop 0
	v_addc_co_u32_e32 v51, vcc, 0, v95, vcc
	v_cvt_pk_bf16_f32 v27, v28, v29
	s_and_b64 vcc, exec, s[4:5]
	global_store_dwordx2 v[40:41], v[26:27], off offset:1536
	global_store_dword v[50:51], v52, off offset:768
	s_cbranch_vccnz .LBB0_16
	v_pk_mul_f32 v[28:29], v[46:47], v[90:91]
	v_mov_b32_e32 v26, v90
	v_pk_mul_f32 v[28:29], v[28:29], v[128:129]
	v_mov_b32_e32 v34, 0
	v_cvt_pk_fp8_f32 v34, v28, v29
	v_mov_b32_e32 v27, v90
	v_pk_mul_f32 v[26:27], v[48:49], v[26:27]
	v_cvt_pk_bf16_f32 v28, v28, v29
	v_pk_mul_f32 v[26:27], v[26:27], v[130:131]
	s_nop 0
	v_cvt_pk_fp8_f32 v34, v26, v27 op_sel:[0,0,1]
	v_cvt_pk_bf16_f32 v29, v26, v27
	global_store_dwordx2 v114, v[28:29], s[14:15] offset:1536
	global_store_dword v[88:89], v34, off offset:768
.LBB0_16:
	v_pk_mul_f32 v[18:19], v[18:19], v[96:97]
	v_pk_mul_f32 v[20:21], v[20:21], v[38:39]
	v_mov_b32_e32 v38, 0
	v_add_co_u32_e32 v34, vcc, 0x4000000, v92
	v_pk_mul_f32 v[18:19], v[18:19], v[132:133]
	s_nop 0
	v_cvt_pk_fp8_f32 v38, v18, v19
	v_pk_mul_f32 v[20:21], v[20:21], v[134:135]
	v_addc_co_u32_e32 v35, vcc, 0, v93, vcc
	v_cvt_pk_fp8_f32 v38, v20, v21 op_sel:[0,0,1]
	v_add_co_u32_e32 v36, vcc, 0x79800000, v94
	v_cvt_pk_bf16_f32 v18, v18, v19
	s_nop 0
	v_addc_co_u32_e32 v37, vcc, 0, v95, vcc
	v_cvt_pk_bf16_f32 v19, v20, v21
	s_and_b64 vcc, exec, s[4:5]
	global_store_dwordx2 v[34:35], v[18:19], off offset:2048
	global_store_dword v[36:37], v38, off offset:1024
	s_cbranch_vccnz .LBB0_18
	v_pk_mul_f32 v[20:21], v[42:43], v[90:91]
	v_mov_b32_e32 v18, v90
	v_pk_mul_f32 v[20:21], v[20:21], v[132:133]
	v_mov_b32_e32 v26, 0
	v_cvt_pk_fp8_f32 v26, v20, v21
	v_mov_b32_e32 v19, v90
	v_pk_mul_f32 v[18:19], v[44:45], v[18:19]
	v_cvt_pk_bf16_f32 v20, v20, v21
	v_pk_mul_f32 v[18:19], v[18:19], v[134:135]
	s_nop 0
	v_cvt_pk_fp8_f32 v26, v18, v19 op_sel:[0,0,1]
	v_cvt_pk_bf16_f32 v21, v18, v19
	global_store_dwordx2 v114, v[20:21], s[14:15] offset:2048
	global_store_dword v[88:89], v26, off offset:1024
.LBB0_18:
	v_pk_mul_f32 v[10:11], v[10:11], v[96:97]
	v_mov_b32_e32 v36, 0
	v_mov_b32_e32 v26, v96
	v_mov_b32_e32 v27, v96
	v_pk_mul_f32 v[12:13], v[12:13], v[26:27]
	v_add_co_u32_e32 v28, vcc, 0x4000000, v92
	v_pk_mul_f32 v[10:11], v[10:11], v[136:137]
	s_nop 0
	v_cvt_pk_fp8_f32 v36, v10, v11
	v_pk_mul_f32 v[12:13], v[12:13], v[138:139]
	v_addc_co_u32_e32 v29, vcc, 0, v93, vcc
	v_cvt_pk_fp8_f32 v36, v12, v13 op_sel:[0,0,1]
	v_add_co_u32_e32 v34, vcc, 0x79800000, v94
	v_cvt_pk_bf16_f32 v10, v10, v11
	s_nop 0
	v_addc_co_u32_e32 v35, vcc, 0, v95, vcc
	v_cvt_pk_bf16_f32 v11, v12, v13
	s_and_b64 vcc, exec, s[4:5]
	global_store_dwordx2 v[28:29], v[10:11], off offset:2560
	global_store_dword v[34:35], v36, off offset:1280
	s_cbranch_vccnz .LBB0_20
	v_pk_mul_f32 v[12:13], v[30:31], v[90:91]
	v_mov_b32_e32 v10, v90
	v_pk_mul_f32 v[12:13], v[12:13], v[136:137]
	v_mov_b32_e32 v18, 0
	v_cvt_pk_fp8_f32 v18, v12, v13
	v_mov_b32_e32 v11, v90
	v_pk_mul_f32 v[10:11], v[32:33], v[10:11]
	v_cvt_pk_bf16_f32 v12, v12, v13
	v_pk_mul_f32 v[10:11], v[10:11], v[138:139]
	s_nop 0
	v_cvt_pk_fp8_f32 v18, v10, v11 op_sel:[0,0,1]
	v_cvt_pk_bf16_f32 v13, v10, v11
	global_store_dwordx2 v114, v[12:13], s[14:15] offset:2560
	global_store_dword v[88:89], v18, off offset:1280
.LBB0_20:
	v_pk_mul_f32 v[6:7], v[6:7], v[96:97]
	v_pk_mul_f32 v[8:9], v[8:9], v[26:27]
	v_mov_b32_e32 v26, 0
	v_add_co_u32_e32 v18, vcc, 0x4000000, v92
	v_pk_mul_f32 v[6:7], v[6:7], v[140:141]
	s_nop 0
	v_cvt_pk_fp8_f32 v26, v6, v7
	v_pk_mul_f32 v[8:9], v[8:9], v[142:143]
	v_addc_co_u32_e32 v19, vcc, 0, v93, vcc
	v_cvt_pk_fp8_f32 v26, v8, v9 op_sel:[0,0,1]
	v_add_co_u32_e32 v20, vcc, 0x79800000, v94
	v_cvt_pk_bf16_f32 v6, v6, v7
	s_nop 0
	v_addc_co_u32_e32 v21, vcc, 0, v95, vcc
	v_cvt_pk_bf16_f32 v7, v8, v9
	s_and_b64 vcc, exec, s[4:5]
	global_store_dwordx2 v[18:19], v[6:7], off offset:3072
	global_store_dword v[20:21], v26, off offset:1536
	s_cbranch_vccnz .LBB0_22
	v_pk_mul_f32 v[8:9], v[22:23], v[90:91]
	v_mov_b32_e32 v6, v90
	v_pk_mul_f32 v[8:9], v[8:9], v[140:141]
	v_mov_b32_e32 v10, 0
	v_cvt_pk_fp8_f32 v10, v8, v9
	v_mov_b32_e32 v7, v90
	v_pk_mul_f32 v[6:7], v[24:25], v[6:7]
	v_cvt_pk_bf16_f32 v8, v8, v9
	v_pk_mul_f32 v[6:7], v[6:7], v[142:143]
	s_nop 0
	v_cvt_pk_fp8_f32 v10, v6, v7 op_sel:[0,0,1]
	v_cvt_pk_bf16_f32 v9, v6, v7
	global_store_dwordx2 v114, v[8:9], s[14:15] offset:3072
	global_store_dword v[88:89], v10, off offset:1536
.LBB0_22:
	v_pk_mul_f32 v[2:3], v[2:3], v[96:97]
	v_mov_b32_e32 v18, 0
	v_mov_b32_e32 v10, v96
	v_mov_b32_e32 v11, v96
	v_pk_mul_f32 v[4:5], v[4:5], v[10:11]
	v_add_co_u32_e32 v12, vcc, 0x4000000, v92
	v_pk_mul_f32 v[2:3], v[2:3], v[144:145]
	s_nop 0
	v_cvt_pk_fp8_f32 v18, v2, v3
	v_pk_mul_f32 v[4:5], v[4:5], v[146:147]
	v_addc_co_u32_e32 v13, vcc, 0, v93, vcc
	v_cvt_pk_fp8_f32 v18, v4, v5 op_sel:[0,0,1]
	v_add_co_u32_e32 v10, vcc, 0x79800000, v94
	v_cvt_pk_bf16_f32 v2, v2, v3
	s_nop 0
	v_addc_co_u32_e32 v11, vcc, 0, v95, vcc
	v_cvt_pk_bf16_f32 v3, v4, v5
	s_and_b64 vcc, exec, s[4:5]
	global_store_dwordx2 v[12:13], v[2:3], off offset:3584
	global_store_dword v[10:11], v18, off offset:1792
	s_cbranch_vccnz .LBB0_7
	v_pk_mul_f32 v[4:5], v[14:15], v[90:91]
	v_mov_b32_e32 v2, v90
	v_pk_mul_f32 v[4:5], v[4:5], v[144:145]
	v_mov_b32_e32 v6, 0
	v_cvt_pk_fp8_f32 v6, v4, v5
	v_mov_b32_e32 v3, v90
	v_pk_mul_f32 v[2:3], v[16:17], v[2:3]
	v_cvt_pk_bf16_f32 v4, v4, v5
	v_pk_mul_f32 v[2:3], v[2:3], v[146:147]
	s_nop 0
	v_cvt_pk_fp8_f32 v6, v2, v3 op_sel:[0,0,1]
	v_cvt_pk_bf16_f32 v5, v2, v3
	global_store_dwordx2 v114, v[4:5], s[14:15] offset:3584
	global_store_dword v[88:89], v6, off offset:1792
	s_branch .LBB0_7

.LBB0_647:
	s_andn2_b64 vcc, exec, s[4:5]
	s_cbranch_vccnz .LBB0_687
	v_ashrrev_i32_e32 v67, 1, v66
	s_add_u32 s13, s84, 0x89800000
	v_lshlrev_b32_e32 v1, 2, v66
	v_and_b32_e32 v102, -8, v67
	v_ashrrev_i32_e32 v67, 3, v66
	s_addc_u32 s14, s85, 0
	v_lshlrev_b32_e32 v68, 4, v66
	v_ashrrev_i32_e32 v104, 4, v66
	v_add_u32_e32 v66, 0x200, v66
	s_mul_i32 s20, s11, 48
	v_and_b32_e32 v1, 60, v1
	s_mul_i32 s12, s11, 0x48
	v_and_b32_e32 v67, -2, v67
	s_movk_i32 s0, 0x104
	s_add_u32 s15, s84, 0x69800000
	v_mov_b32_e32 v101, 0
	v_ashrrev_i32_e32 v106, 4, v66
	s_mul_i32 s18, s11, 0x60
	v_mul_u32_u24_e32 v103, 0x104, v1
	s_addc_u32 s16, s85, 0
	v_and_b32_e32 v98, 0xf0, v68
	v_mov_b32_e32 v99, v101
	v_mul_lo_u32 v105, v104, s0
	v_mul_lo_u32 v107, v106, s0
	s_add_i32 s17, s17, s89
	s_add_i32 s18, s18, s89
	s_add_i32 s19, s12, s89
	s_add_i32 s20, s20, s89
	s_mov_b32 s5, 0
	v_mov_b32_e32 v108, 0x7c
	v_lshlrev_b32_e32 v109, 2, v67
	s_mov_b32 s21, 0
	s_mov_b32 s100, 0
	s_branch .LBB0_651

.LBB0_650:
	s_mov_b32 s100, 1
	s_add_i32 s3, s3, s12
	s_add_i32 s0, s89, s3
	s_sub_i32 s0, s0, 40
	s_cmpk_lt_i32 s0, 0x5d00
	s_cbranch_scc0 .LBB0_687

.LBB0_657:
	s_add_i32 s11, s4, -1
	s_and_b32 s11, s24, s11
	s_ff1_i32_b32 s4, s4
	s_lshl_b32 s25, s11, 6
	s_lshr_b32 s4, s24, s4
	s_lshl_b32 s24, s24, 10
	s_lshl_b32 s11, s11, 5
	s_and_b32 s24, s24, 0x800
	s_and_b32 s11, s11, 0x3f80
	v_bitop3_b32 v67, s25, v108, v1 bitop3:0xc8
	s_add_i32 s11, s11, s24
	v_or_b32_e32 v66, s25, v1
	v_or_b32_e32 v67, s11, v67
	v_cndmask_b32_e64 v100, v66, v67, s[0:1]
	v_lshl_add_u32 v66, s4, 8, v102
	v_mad_i64_i32 v[66:67], s[0:1], s10, v66, 0
	v_lshl_add_u64 v[66:67], v[66:67], 2, s[8:9]
	v_lshl_add_u64 v[66:67], v[100:101], 2, v[66:67]
	s_lshl_b32 s4, s10, 2
	v_lshl_add_u64 v[74:75], v[66:67], 0, s[4:5]
	global_load_dwordx4 v[66:69], v[66:67], off nt
	s_nop 0
	global_load_dwordx4 v[70:73], v[74:75], off nt
	v_lshl_add_u64 v[74:75], v[74:75], 0, s[4:5]
	v_lshl_add_u64 v[82:83], v[74:75], 0, s[4:5]
	global_load_dwordx4 v[74:77], v[74:75], off nt
	s_nop 0
	global_load_dwordx4 v[78:81], v[82:83], off nt
	v_lshl_add_u64 v[82:83], v[82:83], 0, s[4:5]
	v_lshl_add_u64 v[90:91], v[82:83], 0, s[4:5]
	global_load_dwordx4 v[82:85], v[82:83], off nt
	s_nop 0
	global_load_dwordx4 v[86:89], v[90:91], off nt
	v_lshl_add_u64 v[90:91], v[90:91], 0, s[4:5]
	v_lshl_add_u64 v[94:95], v[90:91], 0, s[4:5]
	global_load_dwordx4 v[90:93], v[90:91], off nt
	s_nop 0
	global_load_dwordx4 v[94:97], v[94:95], off nt
	s_cmp_eq_u32 s100, 0
	s_cbranch_scc1 .Lmy_c1_first
	s_waitcnt vmcnt(20)
	s_branch .LBB0_658
.Lmy_c1_first:
	s_waitcnt vmcnt(16)
	s_branch .LBB0_658

.LBB0_668:
	s_add_i32 s11, s4, -1
	s_and_b32 s11, s25, s11
	s_lshl_b32 s24, s11, 6
	v_or_b32_e32 v2, s24, v1
	v_bitop3_b32 v3, s24, v108, v1 bitop3:0xc8
	s_lshl_b32 s24, s25, 10
	s_lshl_b32 s11, s11, 5
	s_and_b32 s24, s24, 0x800
	s_and_b32 s11, s11, 0x3f80
	s_ff1_i32_b32 s4, s4
	s_add_i32 s11, s11, s24
	s_lshr_b32 s4, s25, s4
	v_or_b32_e32 v3, s11, v3
	v_cndmask_b32_e64 v100, v2, v3, s[0:1]
	v_lshl_add_u32 v2, s4, 8, v102
	v_mad_i64_i32 v[2:3], s[0:1], s10, v2, 0
	v_lshl_add_u64 v[2:3], v[2:3], 2, s[8:9]
	v_lshl_add_u64 v[2:3], v[100:101], 2, v[2:3]
	s_lshl_b32 s4, s10, 2
	v_lshl_add_u64 v[10:11], v[2:3], 0, s[4:5]
	global_load_dwordx4 v[6:9], v[2:3], off nt
	s_nop 0
	global_load_dwordx4 v[2:5], v[10:11], off nt
	v_lshl_add_u64 v[10:11], v[10:11], 0, s[4:5]
	v_lshl_add_u64 v[14:15], v[10:11], 0, s[4:5]
	global_load_dwordx4 v[18:21], v[10:11], off nt
	s_nop 0
	global_load_dwordx4 v[10:13], v[14:15], off nt
	v_lshl_add_u64 v[14:15], v[14:15], 0, s[4:5]
	v_lshl_add_u64 v[16:17], v[14:15], 0, s[4:5]
	global_load_dwordx4 v[26:29], v[14:15], off nt
	global_load_dwordx4 v[22:25], v[16:17], off nt
	v_lshl_add_u64 v[14:15], v[16:17], 0, s[4:5]
	v_lshl_add_u64 v[16:17], v[14:15], 0, s[4:5]
	global_load_dwordx4 v[30:33], v[14:15], off nt
	s_nop 0
	global_load_dwordx4 v[14:17], v[16:17], off nt
	s_cmp_eq_u32 s100, 0
	s_cbranch_scc1 .Lmy_c2_first
	s_waitcnt vmcnt(20)
	s_branch .LBB0_669
.Lmy_c2_first:
	s_waitcnt vmcnt(18)
	s_branch .LBB0_669

.LBB0_681:
	s_add_i32 s11, s4, -1
	s_and_b32 s11, s24, s11
	s_ff1_i32_b32 s4, s4
	s_lshl_b32 s25, s11, 6
	s_lshr_b32 s4, s24, s4
	s_lshl_b32 s24, s24, 10
	s_lshl_b32 s11, s11, 5
	s_and_b32 s24, s24, 0x800
	s_and_b32 s11, s11, 0x3f80
	v_bitop3_b32 v35, s25, v108, v1 bitop3:0xc8
	s_add_i32 s11, s11, s24
	v_or_b32_e32 v34, s25, v1
	v_or_b32_e32 v35, s11, v35
	v_cndmask_b32_e64 v100, v34, v35, s[0:1]
	v_lshl_add_u32 v34, s4, 8, v102
	v_mad_i64_i32 v[34:35], s[0:1], s10, v34, 0
	v_lshl_add_u64 v[34:35], v[34:35], 2, s[8:9]
	v_lshl_add_u64 v[34:35], v[100:101], 2, v[34:35]
	s_lshl_b32 s4, s10, 2
	v_lshl_add_u64 v[42:43], v[34:35], 0, s[4:5]
	global_load_dwordx4 v[34:37], v[34:35], off nt
	s_nop 0
	global_load_dwordx4 v[38:41], v[42:43], off nt
	v_lshl_add_u64 v[42:43], v[42:43], 0, s[4:5]
	v_lshl_add_u64 v[50:51], v[42:43], 0, s[4:5]
	global_load_dwordx4 v[42:45], v[42:43], off nt
	s_nop 0
	global_load_dwordx4 v[46:49], v[50:51], off nt
	v_lshl_add_u64 v[50:51], v[50:51], 0, s[4:5]
	v_lshl_add_u64 v[58:59], v[50:51], 0, s[4:5]
	global_load_dwordx4 v[50:53], v[50:51], off nt
	s_nop 0
	global_load_dwordx4 v[54:57], v[58:59], off nt
	v_lshl_add_u64 v[58:59], v[58:59], 0, s[4:5]
	v_lshl_add_u64 v[62:63], v[58:59], 0, s[4:5]
	global_load_dwordx4 v[58:61], v[58:59], off nt
	s_nop 0
	global_load_dwordx4 v[62:65], v[62:63], off nt
	s_waitcnt vmcnt(20)
	s_branch .LBB0_682

.LBB0_1478:
	s_or_b64 exec, exec, s[0:1]
	s_andn2_b64 vcc, exec, s[92:93]
	s_waitcnt lgkmcnt(0)
	s_barrier
	s_cbranch_vccnz .LBB0_1481
	v_and_b32_e32 v1, 63, v0
	v_lshlrev_b32_e32 v2, 2, v0
	v_lshlrev_b32_e32 v16, 3, v1
	v_lshrrev_b32_e32 v0, 2, v0
	v_and_b32_e32 v2, 4, v2
	v_and_b32_e32 v3, 0xf0, v16
	v_and_b32_e32 v0, 8, v0
	v_or3_b32 v4, v3, v0, v2
	v_mbcnt_hi_u32_b32 v0, -1, v228
	v_and_b32_e32 v2, 64, v0
	v_add_u32_e32 v2, 64, v2
	v_xor_b32_e32 v3, 32, v0
	v_cmp_lt_i32_e32 vcc, v3, v2
	s_ashr_i32 s91, s90, 31
	s_ashr_i32 s89, s88, 31
	v_cndmask_b32_e32 v3, v0, v3, vcc
	v_lshlrev_b32_e32 v22, 2, v3
	v_xor_b32_e32 v3, 16, v0
	v_cmp_lt_i32_e32 vcc, v3, v2
	s_lshl_b64 s[6:7], s[90:91], 12
	s_lshl_b64 s[0:1], s[90:91], 6
	v_cndmask_b32_e32 v3, v0, v3, vcc
	v_lshlrev_b32_e32 v23, 2, v3
	v_xor_b32_e32 v3, 8, v0
	v_cmp_lt_i32_e32 vcc, v3, v2
	s_lshl_b64 s[2:3], s[88:89], 6
	v_or_b32_e32 v16, s6, v16
	v_cndmask_b32_e32 v3, v0, v3, vcc
	v_lshlrev_b32_e32 v24, 2, v3
	v_xor_b32_e32 v3, 4, v0
	v_cmp_lt_i32_e32 vcc, v3, v2
	v_mov_b32_e32 v17, s7
	s_lshl_b64 s[6:7], s[88:89], 12
	v_cndmask_b32_e32 v3, v0, v3, vcc
	v_lshlrev_b32_e32 v25, 2, v3
	v_xor_b32_e32 v3, 2, v0
	v_cmp_lt_i32_e32 vcc, v3, v2
	s_lshl_b64 s[8:9], s[90:91], 13
	s_add_u32 s8, s82, s8
	v_cndmask_b32_e32 v3, v0, v3, vcc
	v_lshlrev_b32_e32 v26, 2, v3
	v_xor_b32_e32 v3, 1, v0
	v_cmp_lt_i32_e32 vcc, v3, v2
	s_addc_u32 s9, s83, s9
	v_mov_b32_e32 v28, 0x45200000
	v_cndmask_b32_e32 v0, v0, v3, vcc
	v_lshlrev_b32_e32 v27, 2, v0
	v_lshlrev_b32_e32 v0, 4, v1
	v_mov_b32_e32 v1, 0
	v_or_b32_e32 v2, 0x1000, v0
	v_mov_b32_e32 v3, v1
	v_lshl_add_u64 v[8:9], s[80:81], 0, v[2:3]
	v_or_b32_e32 v2, 0x1400, v0
	v_lshl_add_u64 v[10:11], s[80:81], 0, v[2:3]
	v_or_b32_e32 v2, 0x1800, v0
	v_lshl_add_u64 v[6:7], s[80:81], 0, v[0:1]
	v_mov_b32_e32 v5, v1
	v_lshl_add_u64 v[12:13], s[80:81], 0, v[2:3]
	v_or_b32_e32 v2, 0x1c00, v0
	v_lshl_add_u64 v[0:1], s[8:9], 0, v[0:1]
	s_mov_b64 s[8:9], 0x1000
	v_lshl_add_u64 v[14:15], s[80:81], 0, v[2:3]
	v_lshl_add_u64 v[18:19], v[0:1], 0, s[8:9]
	s_lshl_b64 s[8:9], s[88:89], 13
	s_add_i32 s12, 0, 0x20080
	v_mov_b32_e32 v29, 0x3727c5ac
	global_load_dwordx4 v[196:199], v[6:7], off
	global_load_dwordx4 v[200:203], v[6:7], off offset:1024
	global_load_dwordx4 v[204:207], v[6:7], off offset:2048
	global_load_dwordx4 v[208:211], v[6:7], off offset:3072
	global_load_dwordx4 v[212:215], v[8:9], off
	global_load_dwordx4 v[216:219], v[10:11], off
	global_load_dwordx4 v[220:223], v[12:13], off
	global_load_dwordx4 v[224:227], v[14:15], off
.LBB0_1480:
	v_lshl_add_u64 v[20:21], s[84:85], 0, v[16:17]
	s_add_u32 s10, s84, s0
	v_add_co_u32_e32 v20, vcc, 0x2d400000, v20
	s_addc_u32 s11, s85, s1
	global_load_dwordx3 v[30:32], v28, s[10:11]
	global_load_dwordx3 v[34:36], v28, s[10:11] offset:16
	global_load_dwordx3 v[38:40], v28, s[10:11] offset:32
	global_load_dwordx3 v[42:44], v28, s[10:11] offset:48
	v_addc_co_u32_e32 v21, vcc, 0, v21, vcc
	global_load_dwordx2 v[46:47], v[20:21], off nt
	global_load_dwordx2 v[48:49], v[20:21], off offset:512 nt
	global_load_dwordx2 v[50:51], v[20:21], off offset:1024 nt
	global_load_dwordx2 v[52:53], v[20:21], off offset:1536 nt
	global_load_dwordx2 v[54:55], v[20:21], off offset:2048 nt
	global_load_dwordx2 v[56:57], v[20:21], off offset:2560 nt
	global_load_dwordx2 v[58:59], v[20:21], off offset:3584 nt
	global_load_dwordx2 v[60:61], v[20:21], off offset:3072 nt
	s_add_i32 s90, s90, s88
	s_add_u32 s0, s0, s2
	s_addc_u32 s1, s1, s3
	v_lshl_add_u64 v[16:17], v[16:17], 0, s[6:7]
	s_cmpk_lt_i32 s90, 0x4000
	s_waitcnt vmcnt(7)
	v_and_b32_e32 v45, 0xffff0000, v46
	v_lshlrev_b32_e32 v21, 2, v30
	v_lshlrev_b32_e32 v33, 2, v34
	v_lshlrev_b32_e32 v37, 2, v38
	v_lshlrev_b32_e32 v41, 2, v42
	v_add_u32_e32 v21, s12, v21
	v_add_u32_e32 v33, s12, v33
	v_add_u32_e32 v37, s12, v37
	v_add_u32_e32 v41, s12, v41
	s_waitcnt vmcnt(0)
	v_lshlrev_b32_e32 v72, 16, v60
	v_and_b32_e32 v74, 0xffff0000, v60
	ds_read_b32 v60, v21
	ds_read_b32 v78, v33
	ds_read_b32 v80, v37
	ds_read_b32 v82, v41
	v_lshlrev_b32_e32 v73, 16, v58
	v_and_b32_e32 v75, 0xffff0000, v58
	v_lshlrev_b32_e32 v76, 16, v61
	v_and_b32_e32 v58, 0xffff0000, v61
	s_waitcnt lgkmcnt(3)
	v_ashrrev_i32_e32 v61, 31, v60
	v_ashrrev_i32_e32 v63, 31, v31
	v_mov_b32_e32 v62, v31
	s_waitcnt lgkmcnt(2)
	v_ashrrev_i32_e32 v79, 31, v78
	s_waitcnt lgkmcnt(1)
	v_ashrrev_i32_e32 v81, 31, v80
	s_waitcnt lgkmcnt(0)
	v_ashrrev_i32_e32 v83, 31, v82
	v_lshlrev_b64 v[60:61], 19, v[60:61]
	v_ashrrev_i32_e32 v31, 31, v35
	v_mov_b32_e32 v30, v35
	v_ashrrev_i32_e32 v35, 31, v39
	v_mov_b32_e32 v34, v39
	v_ashrrev_i32_e32 v39, 31, v43
	v_mov_b32_e32 v38, v43
	v_lshlrev_b64 v[42:43], 11, v[62:63]
	v_lshlrev_b64 v[78:79], 19, v[78:79]
	v_lshlrev_b64 v[80:81], 19, v[80:81]
	v_lshlrev_b64 v[82:83], 19, v[82:83]
	v_lshl_add_u64 v[60:61], s[4:5], 0, v[60:61]
	v_lshlrev_b64 v[30:31], 11, v[30:31]
	v_lshlrev_b64 v[34:35], 11, v[34:35]
	v_lshlrev_b64 v[38:39], 11, v[38:39]
	v_lshl_add_u64 v[78:79], s[4:5], 0, v[78:79]
	v_lshl_add_u64 v[80:81], s[4:5], 0, v[80:81]
	v_lshl_add_u64 v[82:83], s[4:5], 0, v[82:83]
	v_lshl_add_u64 v[42:43], v[60:61], 0, v[42:43]
	v_lshl_add_u64 v[30:31], v[78:79], 0, v[30:31]
	v_lshl_add_u64 v[34:35], v[80:81], 0, v[34:35]
	v_lshl_add_u64 v[38:39], v[82:83], 0, v[38:39]
	v_lshl_add_u64 v[42:43], v[42:43], 0, v[4:5]
	v_lshl_add_u64 v[30:31], v[30:31], 0, v[4:5]
	v_lshl_add_u64 v[34:35], v[34:35], 0, v[4:5]
	v_lshl_add_u64 v[38:39], v[38:39], 0, v[4:5]
	global_load_dword v21, v[42:43], off nt
	global_load_dword v33, v[42:43], off offset:256 nt
	global_load_dword v37, v[42:43], off offset:512 nt
	global_load_dword v41, v[42:43], off offset:768 nt
	global_load_dword v86, v[42:43], off offset:1024 nt
	global_load_dword v90, v[42:43], off offset:1280 nt
	global_load_dword v94, v[42:43], off offset:1536 nt
	global_load_dword v98, v[42:43], off offset:1792 nt
	global_load_dword v102, v[30:31], off nt
	global_load_dword v106, v[30:31], off offset:256 nt
	global_load_dword v110, v[30:31], off offset:512 nt
	global_load_dword v114, v[30:31], off offset:768 nt
	global_load_dword v118, v[30:31], off offset:1024 nt
	global_load_dword v122, v[30:31], off offset:1280 nt
	global_load_dword v126, v[30:31], off offset:1536 nt
	global_load_dword v130, v[30:31], off offset:1792 nt
	global_load_dword v134, v[34:35], off nt
	global_load_dword v138, v[34:35], off offset:256 nt
	global_load_dword v142, v[34:35], off offset:512 nt
	global_load_dword v146, v[34:35], off offset:768 nt
	global_load_dword v150, v[34:35], off offset:1024 nt
	global_load_dword v154, v[34:35], off offset:1280 nt
	global_load_dword v158, v[34:35], off offset:1536 nt
	global_load_dword v162, v[34:35], off offset:1792 nt
	global_load_dword v166, v[38:39], off nt
	global_load_dword v170, v[38:39], off offset:256 nt
	global_load_dword v174, v[38:39], off offset:512 nt
	global_load_dword v178, v[38:39], off offset:768 nt
	global_load_dword v182, v[38:39], off offset:1024 nt
	global_load_dword v186, v[38:39], off offset:1280 nt
	global_load_dword v190, v[38:39], off offset:1536 nt
	global_load_dword v194, v[38:39], off offset:1792 nt
	v_mov_b32_e32 v20, v44
	v_lshlrev_b32_e32 v44, 16, v46
	v_lshlrev_b32_e32 v62, 16, v48
	v_and_b32_e32 v63, 0xffff0000, v48
	v_lshlrev_b32_e32 v46, 16, v47
	v_and_b32_e32 v47, 0xffff0000, v47
	v_lshlrev_b32_e32 v48, 16, v49
	v_and_b32_e32 v49, 0xffff0000, v49
	v_lshlrev_b32_e32 v64, 16, v50
	v_and_b32_e32 v65, 0xffff0000, v50
	v_lshlrev_b32_e32 v50, 16, v51
	v_and_b32_e32 v51, 0xffff0000, v51
	v_lshlrev_b32_e32 v66, 16, v52
	v_and_b32_e32 v67, 0xffff0000, v52
	v_lshlrev_b32_e32 v52, 16, v53
	v_and_b32_e32 v53, 0xffff0000, v53
	v_lshlrev_b32_e32 v68, 16, v54
	v_and_b32_e32 v69, 0xffff0000, v54
	v_lshlrev_b32_e32 v54, 16, v55
	v_and_b32_e32 v55, 0xffff0000, v55
	v_lshlrev_b32_e32 v70, 16, v56
	v_and_b32_e32 v71, 0xffff0000, v56
	v_lshlrev_b32_e32 v56, 16, v57
	v_and_b32_e32 v57, 0xffff0000, v57
	v_lshlrev_b32_e32 v77, 16, v59
	v_and_b32_e32 v59, 0xffff0000, v59
	s_waitcnt vmcnt(31)
	v_cvt_pk_f32_fp8_e32 v[30:31], v21
	s_waitcnt vmcnt(30)
	v_cvt_pk_f32_fp8_e32 v[38:39], v33
	v_cvt_pk_f32_fp8_sdwa v[34:35], v21 src0_sel:WORD_1
	v_cvt_pk_f32_fp8_sdwa v[42:43], v33 src0_sel:WORD_1
	s_waitcnt vmcnt(29)
	v_cvt_pk_f32_fp8_e32 v[60:61], v37
	v_cvt_pk_f32_fp8_sdwa v[78:79], v37 src0_sel:WORD_1
	s_waitcnt vmcnt(28)
	v_cvt_pk_f32_fp8_e32 v[80:81], v41
	v_cvt_pk_f32_fp8_sdwa v[82:83], v41 src0_sel:WORD_1
	s_waitcnt vmcnt(27)
	v_cvt_pk_f32_fp8_e32 v[84:85], v86
	v_cvt_pk_f32_fp8_sdwa v[86:87], v86 src0_sel:WORD_1
	s_waitcnt vmcnt(26)
	v_cvt_pk_f32_fp8_e32 v[88:89], v90
	s_waitcnt vmcnt(25)
	v_cvt_pk_f32_fp8_e32 v[92:93], v94
	v_cvt_pk_f32_fp8_sdwa v[94:95], v94 src0_sel:WORD_1
	s_waitcnt vmcnt(24)
	v_cvt_pk_f32_fp8_e32 v[96:97], v98
	v_cvt_pk_f32_fp8_sdwa v[98:99], v98 src0_sel:WORD_1
	s_waitcnt vmcnt(23)
	v_cvt_pk_f32_fp8_e32 v[100:101], v102
	s_waitcnt vmcnt(22)
	v_cvt_pk_f32_fp8_e32 v[104:105], v106
	v_cvt_pk_f32_fp8_sdwa v[90:91], v90 src0_sel:WORD_1
	v_cvt_pk_f32_fp8_sdwa v[102:103], v102 src0_sel:WORD_1
	v_cvt_pk_f32_fp8_sdwa v[106:107], v106 src0_sel:WORD_1
	s_waitcnt vmcnt(21)
	v_cvt_pk_f32_fp8_e32 v[108:109], v110
	v_cvt_pk_f32_fp8_sdwa v[110:111], v110 src0_sel:WORD_1
	s_waitcnt vmcnt(20)
	v_cvt_pk_f32_fp8_e32 v[112:113], v114
	v_cvt_pk_f32_fp8_sdwa v[114:115], v114 src0_sel:WORD_1
	s_waitcnt vmcnt(19)
	v_cvt_pk_f32_fp8_e32 v[116:117], v118
	v_cvt_pk_f32_fp8_sdwa v[118:119], v118 src0_sel:WORD_1
	s_waitcnt vmcnt(18)
	v_cvt_pk_f32_fp8_e32 v[120:121], v122
	s_waitcnt vmcnt(17)
	v_cvt_pk_f32_fp8_e32 v[124:125], v126
	v_cvt_pk_f32_fp8_sdwa v[126:127], v126 src0_sel:WORD_1
	s_waitcnt vmcnt(16)
	v_cvt_pk_f32_fp8_e32 v[128:129], v130
	v_cvt_pk_f32_fp8_sdwa v[130:131], v130 src0_sel:WORD_1
	s_waitcnt vmcnt(15)
	v_cvt_pk_f32_fp8_e32 v[132:133], v134
	s_waitcnt vmcnt(14)
	v_cvt_pk_f32_fp8_e32 v[136:137], v138
	v_cvt_pk_f32_fp8_sdwa v[122:123], v122 src0_sel:WORD_1
	v_cvt_pk_f32_fp8_sdwa v[134:135], v134 src0_sel:WORD_1
	v_cvt_pk_f32_fp8_sdwa v[138:139], v138 src0_sel:WORD_1
	s_waitcnt vmcnt(13)
	v_cvt_pk_f32_fp8_e32 v[140:141], v142
	v_cvt_pk_f32_fp8_sdwa v[142:143], v142 src0_sel:WORD_1
	s_waitcnt vmcnt(12)
	v_cvt_pk_f32_fp8_e32 v[144:145], v146
	v_cvt_pk_f32_fp8_sdwa v[146:147], v146 src0_sel:WORD_1
	s_waitcnt vmcnt(11)
	v_cvt_pk_f32_fp8_e32 v[148:149], v150
	v_cvt_pk_f32_fp8_sdwa v[150:151], v150 src0_sel:WORD_1
	s_waitcnt vmcnt(10)
	v_cvt_pk_f32_fp8_e32 v[152:153], v154
	s_waitcnt vmcnt(9)
	v_cvt_pk_f32_fp8_e32 v[156:157], v158
	v_cvt_pk_f32_fp8_sdwa v[158:159], v158 src0_sel:WORD_1
	s_waitcnt vmcnt(8)
	v_cvt_pk_f32_fp8_e32 v[160:161], v162
	v_cvt_pk_f32_fp8_sdwa v[162:163], v162 src0_sel:WORD_1
	s_waitcnt vmcnt(7)
	v_cvt_pk_f32_fp8_e32 v[164:165], v166
	s_waitcnt vmcnt(6)
	v_cvt_pk_f32_fp8_e32 v[168:169], v170
	v_cvt_pk_f32_fp8_sdwa v[154:155], v154 src0_sel:WORD_1
	v_cvt_pk_f32_fp8_sdwa v[166:167], v166 src0_sel:WORD_1
	v_cvt_pk_f32_fp8_sdwa v[170:171], v170 src0_sel:WORD_1
	s_waitcnt vmcnt(5)
	v_cvt_pk_f32_fp8_e32 v[172:173], v174
	v_cvt_pk_f32_fp8_sdwa v[174:175], v174 src0_sel:WORD_1
	s_waitcnt vmcnt(4)
	v_cvt_pk_f32_fp8_e32 v[176:177], v178
	v_cvt_pk_f32_fp8_sdwa v[178:179], v178 src0_sel:WORD_1
	s_waitcnt vmcnt(3)
	v_cvt_pk_f32_fp8_e32 v[180:181], v182
	v_cvt_pk_f32_fp8_sdwa v[182:183], v182 src0_sel:WORD_1
	s_waitcnt vmcnt(2)
	v_cvt_pk_f32_fp8_e32 v[184:185], v186
	v_pk_fma_f32 v[30:31], v[32:33], v[30:31], v[44:45] op_sel_hi:[0,1,1]
	v_pk_fma_f32 v[38:39], v[32:33], v[38:39], v[62:63] op_sel_hi:[0,1,1]
	v_pk_fma_f32 v[34:35], v[32:33], v[34:35], v[46:47] op_sel_hi:[0,1,1]
	v_pk_fma_f32 v[42:43], v[32:33], v[42:43], v[48:49] op_sel_hi:[0,1,1]
	v_pk_fma_f32 v[44:45], v[32:33], v[60:61], v[64:65] op_sel_hi:[0,1,1]
	v_pk_fma_f32 v[46:47], v[32:33], v[78:79], v[50:51] op_sel_hi:[0,1,1]
	v_pk_fma_f32 v[48:49], v[32:33], v[80:81], v[66:67] op_sel_hi:[0,1,1]
	v_pk_fma_f32 v[50:51], v[32:33], v[82:83], v[52:53] op_sel_hi:[0,1,1]
	v_pk_fma_f32 v[52:53], v[32:33], v[84:85], v[68:69] op_sel_hi:[0,1,1]
	v_pk_fma_f32 v[54:55], v[32:33], v[86:87], v[54:55] op_sel_hi:[0,1,1]
	v_pk_fma_f32 v[60:61], v[32:33], v[88:89], v[70:71] op_sel_hi:[0,1,1]
	v_mov_b32_e32 v62, v92
	v_mov_b32_e32 v63, v96
	v_mov_b32_e32 v96, v93
	v_mov_b32_e32 v64, v94
	v_mov_b32_e32 v65, v98
	v_mov_b32_e32 v98, v95
	v_pk_fma_f32 v[30:31], v[36:37], v[100:101], v[30:31] op_sel_hi:[0,1,1]
	v_pk_fma_f32 v[38:39], v[36:37], v[104:105], v[38:39] op_sel_hi:[0,1,1]
	v_pk_fma_f32 v[56:57], v[32:33], v[90:91], v[56:57] op_sel_hi:[0,1,1]
	v_mov_b32_e32 v66, v124
	v_mov_b32_e32 v67, v128
	v_mov_b32_e32 v128, v125
	v_mov_b32_e32 v68, v126
	v_mov_b32_e32 v69, v130
	v_mov_b32_e32 v130, v127
	v_pk_fma_f32 v[34:35], v[36:37], v[102:103], v[34:35] op_sel_hi:[0,1,1]
	v_pk_fma_f32 v[42:43], v[36:37], v[106:107], v[42:43] op_sel_hi:[0,1,1]
	v_pk_fma_f32 v[44:45], v[36:37], v[108:109], v[44:45] op_sel_hi:[0,1,1]
	v_pk_fma_f32 v[46:47], v[36:37], v[110:111], v[46:47] op_sel_hi:[0,1,1]
	v_pk_fma_f32 v[48:49], v[36:37], v[112:113], v[48:49] op_sel_hi:[0,1,1]
	v_pk_fma_f32 v[50:51], v[36:37], v[114:115], v[50:51] op_sel_hi:[0,1,1]
	v_pk_fma_f32 v[52:53], v[36:37], v[116:117], v[52:53] op_sel_hi:[0,1,1]
	v_pk_fma_f32 v[54:55], v[36:37], v[118:119], v[54:55] op_sel_hi:[0,1,1]
	v_pk_fma_f32 v[60:61], v[36:37], v[120:121], v[60:61] op_sel_hi:[0,1,1]
	v_pk_fma_f32 v[62:63], v[32:33], v[62:63], v[72:73] op_sel_hi:[0,1,1]
	v_pk_fma_f32 v[72:73], v[32:33], v[96:97], v[74:75] op_sel_hi:[0,1,1]
	v_pk_fma_f32 v[64:65], v[32:33], v[64:65], v[76:77] op_sel_hi:[0,1,1]
	v_pk_fma_f32 v[32:33], v[32:33], v[98:99], v[58:59] op_sel_hi:[0,1,1]
	v_pk_fma_f32 v[30:31], v[40:41], v[132:133], v[30:31] op_sel_hi:[0,1,1]
	v_pk_fma_f32 v[38:39], v[40:41], v[136:137], v[38:39] op_sel_hi:[0,1,1]
	s_waitcnt vmcnt(1)
	v_cvt_pk_f32_fp8_e32 v[188:189], v190
	s_waitcnt vmcnt(0)
	v_cvt_pk_f32_fp8_e32 v[192:193], v194
	v_mov_b32_e32 v70, v156
	v_mov_b32_e32 v71, v160
	v_mov_b32_e32 v160, v157
	v_mov_b32_e32 v78, v158
	v_mov_b32_e32 v79, v162
	v_mov_b32_e32 v162, v159
	v_pk_fma_f32 v[56:57], v[36:37], v[122:123], v[56:57] op_sel_hi:[0,1,1]
	v_pk_fma_f32 v[34:35], v[40:41], v[134:135], v[34:35] op_sel_hi:[0,1,1]
	v_pk_fma_f32 v[42:43], v[40:41], v[138:139], v[42:43] op_sel_hi:[0,1,1]
	v_pk_fma_f32 v[44:45], v[40:41], v[140:141], v[44:45] op_sel_hi:[0,1,1]
	v_pk_fma_f32 v[46:47], v[40:41], v[142:143], v[46:47] op_sel_hi:[0,1,1]
	v_pk_fma_f32 v[48:49], v[40:41], v[144:145], v[48:49] op_sel_hi:[0,1,1]
	v_pk_fma_f32 v[50:51], v[40:41], v[146:147], v[50:51] op_sel_hi:[0,1,1]
	v_pk_fma_f32 v[52:53], v[40:41], v[148:149], v[52:53] op_sel_hi:[0,1,1]
	v_pk_fma_f32 v[54:55], v[40:41], v[150:151], v[54:55] op_sel_hi:[0,1,1]
	v_pk_fma_f32 v[58:59], v[40:41], v[152:153], v[60:61] op_sel_hi:[0,1,1]
	v_pk_fma_f32 v[60:61], v[36:37], v[66:67], v[62:63] op_sel_hi:[0,1,1]
	v_pk_fma_f32 v[62:63], v[36:37], v[128:129], v[72:73] op_sel_hi:[0,1,1]
	v_pk_fma_f32 v[64:65], v[36:37], v[68:69], v[64:65] op_sel_hi:[0,1,1]
	v_pk_fma_f32 v[32:33], v[36:37], v[130:131], v[32:33] op_sel_hi:[0,1,1]
	v_pk_fma_f32 v[30:31], v[20:21], v[164:165], v[30:31] op_sel_hi:[0,1,1]
	v_pk_fma_f32 v[36:37], v[20:21], v[168:169], v[38:39] op_sel_hi:[0,1,1]
	v_cvt_pk_f32_fp8_sdwa v[186:187], v186 src0_sel:WORD_1
	v_cvt_pk_f32_fp8_sdwa v[190:191], v190 src0_sel:WORD_1
	v_cvt_pk_f32_fp8_sdwa v[194:195], v194 src0_sel:WORD_1
	v_pk_fma_f32 v[56:57], v[40:41], v[154:155], v[56:57] op_sel_hi:[0,1,1]
	v_pk_fma_f32 v[34:35], v[20:21], v[166:167], v[34:35] op_sel_hi:[0,1,1]
	v_pk_fma_f32 v[38:39], v[20:21], v[170:171], v[42:43] op_sel_hi:[0,1,1]
	v_pk_fma_f32 v[42:43], v[20:21], v[172:173], v[44:45] op_sel_hi:[0,1,1]
	v_pk_fma_f32 v[44:45], v[20:21], v[174:175], v[46:47] op_sel_hi:[0,1,1]
	v_pk_fma_f32 v[46:47], v[20:21], v[176:177], v[48:49] op_sel_hi:[0,1,1]
	v_pk_fma_f32 v[48:49], v[20:21], v[178:179], v[50:51] op_sel_hi:[0,1,1]
	v_pk_fma_f32 v[50:51], v[20:21], v[180:181], v[52:53] op_sel_hi:[0,1,1]
	v_pk_fma_f32 v[52:53], v[20:21], v[182:183], v[54:55] op_sel_hi:[0,1,1]
	v_pk_fma_f32 v[54:55], v[20:21], v[184:185], v[58:59] op_sel_hi:[0,1,1]
	v_pk_fma_f32 v[58:59], v[40:41], v[70:71], v[60:61] op_sel_hi:[0,1,1]
	v_pk_fma_f32 v[60:61], v[40:41], v[160:161], v[62:63] op_sel_hi:[0,1,1]
	v_pk_fma_f32 v[62:63], v[40:41], v[78:79], v[64:65] op_sel_hi:[0,1,1]
	v_pk_fma_f32 v[32:33], v[40:41], v[162:163], v[32:33] op_sel_hi:[0,1,1]
	v_pk_mul_f32 v[40:41], v[30:31], v[30:31]
	v_pk_mul_f32 v[66:67], v[36:37], v[36:37]
	v_pk_mul_f32 v[64:65], v[34:35], v[34:35]
	v_pk_mul_f32 v[68:69], v[38:39], v[38:39]
	v_pk_mul_f32 v[70:71], v[42:43], v[42:43]
	v_add_f32_e32 v66, v66, v67
	v_add_f32_e32 v40, v40, v41
	v_pk_mul_f32 v[72:73], v[44:45], v[44:45]
	v_pk_mul_f32 v[74:75], v[46:47], v[46:47]
	v_add_f32_e32 v41, v70, v71
	v_add_f32_e32 v66, v68, v66
	v_add_f32_e32 v40, v64, v40
	v_mov_b32_e32 v81, v192
	v_mov_b32_e32 v192, v189
	v_pk_mul_f32 v[76:77], v[48:49], v[48:49]
	v_pk_mul_f32 v[78:79], v[50:51], v[50:51]
	v_add_f32_e32 v67, v74, v75
	v_add_f32_e32 v41, v72, v41
	v_add_f32_e32 v66, v69, v66
	v_add_f32_e32 v40, v65, v40
	v_mov_b32_e32 v80, v188
	v_mov_b32_e32 v82, v190
	v_mov_b32_e32 v83, v194
	v_mov_b32_e32 v194, v191
	v_pk_fma_f32 v[56:57], v[20:21], v[186:187], v[56:57] op_sel_hi:[0,1,1]
	v_pk_mul_f32 v[84:85], v[52:53], v[52:53]
	v_pk_mul_f32 v[86:87], v[54:55], v[54:55]
	v_pk_fma_f32 v[60:61], v[20:21], v[192:193], v[60:61] op_sel_hi:[0,1,1]
	v_add_f32_e32 v70, v78, v79
	v_add_f32_e32 v64, v76, v67
	v_add_f32_e32 v41, v73, v41
	v_add_f32_e32 v40, v40, v66
	v_pk_mul_f32 v[88:89], v[56:57], v[56:57]
	v_pk_fma_f32 v[58:59], v[20:21], v[80:81], v[58:59] op_sel_hi:[0,1,1]
	v_pk_fma_f32 v[62:63], v[20:21], v[82:83], v[62:63] op_sel_hi:[0,1,1]
	v_pk_fma_f32 v[20:21], v[20:21], v[194:195], v[32:33] op_sel_hi:[0,1,1]
	v_pk_mul_f32 v[32:33], v[60:61], v[60:61]
	v_add_f32_e32 v71, v86, v87
	v_add_f32_e32 v67, v84, v70
	v_add_f32_e32 v64, v77, v64
	v_add_f32_e32 v40, v40, v41
	v_pk_fma_f32 v[32:33], v[58:59], v[58:59], v[32:33]
	v_add_f32_e32 v68, v88, v71
	v_add_f32_e32 v65, v85, v67
	v_add_f32_e32 v40, v40, v64
	v_pk_fma_f32 v[32:33], v[62:63], v[62:63], v[32:33]
	v_add_f32_e32 v67, v89, v68
	v_add_f32_e32 v40, v40, v65
	v_pk_fma_f32 v[32:33], v[20:21], v[20:21], v[32:33]
	v_add_f32_e32 v40, v40, v67
	v_add_f32_e32 v32, v40, v32
	v_add_f32_e32 v32, v32, v33
	ds_bpermute_b32 v33, v22, v32
	s_waitcnt lgkmcnt(0)
	v_add_f32_e32 v32, v32, v33
	ds_bpermute_b32 v33, v23, v32
	s_waitcnt lgkmcnt(0)
	v_add_f32_e32 v32, v32, v33
	ds_bpermute_b32 v33, v24, v32
	s_waitcnt lgkmcnt(0)
	v_add_f32_e32 v32, v32, v33
	ds_bpermute_b32 v33, v25, v32
	s_waitcnt lgkmcnt(0)
	v_add_f32_e32 v32, v32, v33
	ds_bpermute_b32 v33, v26, v32
	s_waitcnt lgkmcnt(0)
	v_add_f32_e32 v32, v32, v33
	ds_bpermute_b32 v33, v27, v32
	s_waitcnt lgkmcnt(0)
	v_add_f32_e32 v32, v32, v33
	v_fmamk_f32 v32, v32, 0x3a000000, v29
	v_rsq_f32_e32 v32, v32
	s_nop 0
	v_pk_mul_f32 v[30:31], v[30:31], v[32:33] op_sel_hi:[1,0]
	v_pk_mul_f32 v[34:35], v[34:35], v[32:33] op_sel_hi:[1,0]
	v_pk_mul_f32 v[0:1], v[196:197], v[30:31]
	v_pk_mul_f32 v[2:3], v[198:199], v[34:35]
	global_store_dwordx4 v[18:19], v[0:3], off offset:-4096 nt
	v_pk_mul_f32 v[30:31], v[38:39], v[32:33] op_sel_hi:[1,0]
	v_pk_mul_f32 v[34:35], v[36:37], v[32:33] op_sel_hi:[1,0]
	v_pk_mul_f32 v[2:3], v[202:203], v[30:31]
	v_pk_mul_f32 v[0:1], v[200:201], v[34:35]
	global_store_dwordx4 v[18:19], v[0:3], off offset:-3072 nt
	v_pk_mul_f32 v[30:31], v[44:45], v[32:33] op_sel_hi:[1,0]
	v_pk_mul_f32 v[34:35], v[42:43], v[32:33] op_sel_hi:[1,0]
	v_pk_mul_f32 v[2:3], v[206:207], v[30:31]
	v_pk_mul_f32 v[0:1], v[204:205], v[34:35]
	global_store_dwordx4 v[18:19], v[0:3], off offset:-2048 nt
	v_pk_mul_f32 v[30:31], v[48:49], v[32:33] op_sel_hi:[1,0]
	v_pk_mul_f32 v[34:35], v[46:47], v[32:33] op_sel_hi:[1,0]
	v_pk_mul_f32 v[2:3], v[210:211], v[30:31]
	v_pk_mul_f32 v[0:1], v[208:209], v[34:35]
	global_store_dwordx4 v[18:19], v[0:3], off offset:-1024 nt
	v_pk_mul_f32 v[30:31], v[52:53], v[32:33] op_sel_hi:[1,0]
	v_pk_mul_f32 v[34:35], v[50:51], v[32:33] op_sel_hi:[1,0]
	v_pk_mul_f32 v[2:3], v[214:215], v[30:31]
	v_pk_mul_f32 v[0:1], v[212:213], v[34:35]
	global_store_dwordx4 v[18:19], v[0:3], off nt
	v_pk_mul_f32 v[30:31], v[56:57], v[32:33] op_sel_hi:[1,0]
	v_pk_mul_f32 v[34:35], v[54:55], v[32:33] op_sel_hi:[1,0]
	v_pk_mul_f32 v[2:3], v[218:219], v[30:31]
	v_pk_mul_f32 v[0:1], v[216:217], v[34:35]
	global_store_dwordx4 v[18:19], v[0:3], off offset:1024 nt
	v_mov_b32_e32 v30, v62
	v_mov_b32_e32 v31, v20
	v_mov_b32_e32 v34, v58
	v_mov_b32_e32 v35, v60
	v_pk_mul_f32 v[30:31], v[30:31], v[32:33] op_sel_hi:[1,0]
	v_pk_mul_f32 v[34:35], v[34:35], v[32:33] op_sel_hi:[1,0]
	v_mov_b32_e32 v60, v59
	v_mov_b32_e32 v20, v63
	v_pk_mul_f32 v[20:21], v[20:21], v[32:33] op_sel_hi:[1,0]
	v_pk_mul_f32 v[0:1], v[34:35], v[220:221]
	v_pk_mul_f32 v[2:3], v[30:31], v[222:223]
	global_store_dwordx4 v[18:19], v[0:3], off offset:2048 nt
	s_nop 0
	v_pk_mul_f32 v[30:31], v[60:61], v[32:33] op_sel_hi:[1,0]
	v_pk_mul_f32 v[2:3], v[20:21], v[226:227]
	v_pk_mul_f32 v[0:1], v[30:31], v[224:225]
	global_store_dwordx4 v[18:19], v[0:3], off offset:3072 nt
	v_lshl_add_u64 v[18:19], v[18:19], 0, s[8:9]
	s_cbranch_scc1 .LBB0_1480

	.amdhsa_kernel _Z3fwd6Params
		.amdhsa_group_segment_fixed_size 0
		.amdhsa_private_segment_fixed_size 0
		.amdhsa_kernarg_size 480
		.amdhsa_user_sgpr_count 2
		.amdhsa_user_sgpr_dispatch_ptr 0
		.amdhsa_user_sgpr_queue_ptr 0
		.amdhsa_user_sgpr_kernarg_segment_ptr 1
		.amdhsa_user_sgpr_dispatch_id 0
		.amdhsa_user_sgpr_kernarg_preload_length 0
		.amdhsa_user_sgpr_kernarg_preload_offset 0
		.amdhsa_user_sgpr_private_segment_size 0
		.amdhsa_uses_dynamic_stack 0
		.amdhsa_enable_private_segment 0
		.amdhsa_system_sgpr_workgroup_id_x 1
		.amdhsa_system_sgpr_workgroup_id_y 0
		.amdhsa_system_sgpr_workgroup_id_z 0
		.amdhsa_system_sgpr_workgroup_info 0
		.amdhsa_system_vgpr_workitem_id 0
		.amdhsa_next_free_vgpr 253
		.amdhsa_next_free_sgpr 102
		.amdhsa_accum_offset 256
		.amdhsa_reserve_vcc 1
		.amdhsa_float_round_mode_32 0
		.amdhsa_float_round_mode_16_64 0
		.amdhsa_float_denorm_mode_32 3
		.amdhsa_float_denorm_mode_16_64 3
		.amdhsa_dx10_clamp 1
		.amdhsa_ieee_mode 1
		.amdhsa_fp16_overflow 0
		.amdhsa_tg_split 0
		.amdhsa_exception_fp_ieee_invalid_op 0
		.amdhsa_exception_fp_denorm_src 0
		.amdhsa_exception_fp_ieee_div_zero 0
		.amdhsa_exception_fp_ieee_overflow 0
		.amdhsa_exception_fp_ieee_underflow 0
		.amdhsa_exception_fp_ieee_inexact 0
		.amdhsa_exception_int_div_zero 0
	.end_amdhsa_kernel

amdhsa.kernels:
  - .agpr_count:     0
    .args:
      - .offset:         0
        .size:           224
        .value_kind:     by_value
      - .offset:         224
        .size:           4
        .value_kind:     hidden_block_count_x
      - .offset:         228
        .size:           4
        .value_kind:     hidden_block_count_y
      - .offset:         232
        .size:           4
        .value_kind:     hidden_block_count_z
      - .offset:         236
        .size:           2
        .value_kind:     hidden_group_size_x
      - .offset:         238
        .size:           2
        .value_kind:     hidden_group_size_y
      - .offset:         240
        .size:           2
        .value_kind:     hidden_group_size_z
      - .offset:         242
        .size:           2
        .value_kind:     hidden_remainder_x
      - .offset:         244
        .size:           2
        .value_kind:     hidden_remainder_y
      - .offset:         246
        .size:           2
        .value_kind:     hidden_remainder_z
      - .offset:         264
        .size:           8
        .value_kind:     hidden_global_offset_x
      - .offset:         272
        .size:           8
        .value_kind:     hidden_global_offset_y
      - .offset:         280
        .size:           8
        .value_kind:     hidden_global_offset_z
      - .offset:         288
        .size:           2
        .value_kind:     hidden_grid_dims
      - .offset:         344
        .size:           4
        .value_kind:     hidden_dynamic_lds_size
    .group_segment_fixed_size: 0
    .kernarg_segment_align: 8
    .kernarg_segment_size: 480
    .language:       OpenCL C
    .language_version:
      - 2
      - 0
    .max_flat_workgroup_size: 512
    .name:           _Z3fwd6Params
    .private_segment_fixed_size: 0
    .sgpr_count:     108
    .sgpr_spill_count: 109
    .symbol:         _Z3fwd6Params.kd
    .uniform_work_group_size: 1
    .uses_dynamic_stack: false
    .vgpr_count:     253
    .vgpr_spill_count: 0
    .wavefront_size: 64
